# baseline (speedup 1.0000x reference)
.Las_set:
	s_sub_u32 s96, s96, 4
	s_cmp_ge_i32 s48, s47
	s_cbranch_scc1 .LBB2_78
	s_add_i32 s101, s48, 64
	s_sub_i32 s3, s47, s5
	s_cmp_lg_u32 s3, 0x70
	s_cbranch_scc1 .Lperm_done
	s_cmp_lt_u32 s2, 9
	s_cbranch_scc0 .Lperm_r1b
	s_mul_i32 s3, s2, 7
	s_add_i32 s3, s3, 6
	s_branch .Lperm_r1d
.Lperm_r1b:
	s_sub_i32 s3, s2, 9
	s_mul_hi_u32 s4, s3, 0xaaaaaaab
	s_lshr_b32 s4, s4, 2
	s_add_i32 s3, s3, s4
.Lperm_r1d:
	s_add_i32 s48, s5, s3
	s_cmp_ge_u32 s2, 48
	s_cbranch_scc1 .Lperm_done
	s_sub_i32 s3, s2, 9
	s_cmp_lt_u32 s3, 7
	s_cbranch_scc0 .Lperm_r2b
	s_mul_i32 s3, s3, 7
	s_add_i32 s3, s3, 5
	s_branch .Lperm_r2d
.Lperm_r2b:
	s_add_i32 s3, s3, 2
	s_cmp_lt_u32 s2, 9
	s_cselect_b32 s3, s2, s3
	s_mul_hi_u32 s4, s3, 0xaaaaaaab
	s_lshr_b32 s4, s4, 2
	s_mul_i32 s99, s4, 6
	s_sub_i32 s99, s3, s99
	s_mul_i32 s3, s4, 7
	s_cmp_lt_u32 s99, 5
	s_cselect_b32 s99, s99, 6
	s_add_i32 s3, s3, s99
.Lperm_r2d:
	s_add_i32 s101, s5, s3
	s_add_i32 s101, s101, 64
.Lperm_done:
	s_load_dword s13, s[0:1], 0x38
	s_load_dwordx2 s[2:3], s[0:1], 0x30
	s_load_dwordx8 s[4:11], s[0:1], 0x0
	v_bfe_u32 v1, v0, 4, 2
	v_lshrrev_b32_e32 v2, 5, v0
	s_waitcnt lgkmcnt(0)
	s_lshr_b32 s49, s13, 3
	s_bfe_u32 s1, s12, 0x10006
	v_and_or_b32 v2, v2, 4, v1
	v_lshrrev_b32_e32 v5, 7, v0
	s_cmpk_lt_u32 s12, 0x80
	v_lshlrev_b32_e32 v2, 4, v2
	v_lshlrev_b32_e32 v3, 3, v0
	s_movk_i32 s0, 0x78
	v_bfe_u32 v4, v0, 4, 3
	v_bitop3_b32 v5, v5, v0, 7 bitop3:0x78
	v_lshlrev_b32_e32 v6, 6, v0
	s_cselect_b64 s[12:13], -1, 0
	v_bitop3_b32 v2, v2, v3, s0 bitop3:0x78
	v_xor_b32_e32 v5, v5, v4
	s_lshl_b32 s0, s1, 6
	v_lshlrev_b32_e32 v4, 2, v1
	v_lshlrev_b32_e32 v1, 11, v1
	v_and_b32_e32 v6, 0x300, v6
	v_and_b32_e32 v8, 8, v3
	v_lshrrev_b32_e32 v101, 4, v0
	v_and_b32_e32 v103, 15, v0
	v_lshrrev_b32_e32 v124, 3, v0
	v_lshl_add_u32 v125, v0, 4, 0
	v_or3_b32 v1, v1, v6, v8
	v_bfe_u32 v6, v0, 1, 3
	v_or_b32_e32 v0, s0, v4
	v_and_b32_e32 v7, 0xe0, v3
	v_lshl_add_u32 v100, v0, 1, 0
	s_lshl_b32 s1, s1, 7
	v_and_b32_e32 v0, 16, v3
	v_or_b32_e32 v3, s1, v0
	v_bitop3_b32 v0, s1, v7, v0 bitop3:0x36
	v_or_b32_e32 v127, v0, v1
	v_bitop3_b32 v0, v3, v7, 32 bitop3:0x36
	v_or_b32_e32 v128, v0, v1
	v_bitop3_b32 v0, v3, v7, 64 bitop3:0x36
	s_movk_i32 s1, 0x60
	v_or_b32_e32 v129, v0, v1
	v_bitop3_b32 v0, v3, v7, s1 bitop3:0x36
	s_add_i32 s1, s23, 15
	s_lshr_b32 s1, s1, 4
	v_or_b32_e32 v130, v0, v1
	s_add_i32 s1, s39, s1
	v_cvt_f32_i32_e32 v0, s39
	s_add_i32 s1, s1, -1
	v_cvt_f32_i32_e32 v1, s1
	s_add_i32 s14, s25, 15
	v_rcp_iflag_f32_e32 v144, v0
	s_lshr_b32 s14, s14, 4
	v_add_f32_e32 v0, 0.5, v1
	v_cvt_f32_i32_e32 v1, s40
	s_add_i32 s14, s40, s14
	s_add_i32 s14, s14, -1
	v_mul_f32_e32 v0, v144, v0
	v_cvt_i32_f32_e32 v0, v0
	v_cvt_f32_i32_e32 v7, s14
	v_rcp_iflag_f32_e32 v145, v1
	s_add_i32 s16, s27, 15
	s_lshr_b32 s16, s16, 4
	v_cvt_f32_i32_e32 v1, s41
	s_add_i32 s16, s41, s16
	v_readfirstlane_b32 s1, v0
	v_add_f32_e32 v0, 0.5, v7
	s_add_i32 s16, s16, -1
	s_add_i32 s17, s29, 15
	s_add_i32 s18, s31, 15
	s_add_i32 s19, s33, 15
	s_add_i32 s20, s35, 15
	s_add_i32 s21, s38, 15
	v_mul_f32_e32 v0, v145, v0
	s_lshr_b32 s17, s17, 4
	s_lshr_b32 s18, s18, 4
	s_lshr_b32 s19, s19, 4
	s_lshr_b32 s20, s20, 4
	s_lshr_b32 s21, s21, 4
	v_cvt_i32_f32_e32 v0, v0
	v_cvt_f32_i32_e32 v7, s16
	s_add_i32 s17, s42, s17
	s_add_i32 s18, s43, s18
	s_add_i32 s19, s44, s19
	s_add_i32 s20, s45, s20
	s_add_i32 s21, s46, s21
	v_rcp_iflag_f32_e32 v146, v1
	s_add_i32 s50, 0, 0xe000
	s_lshl_b32 s52, s39, 4
	s_lshl_b32 s53, s40, 4
	s_lshl_b32 s54, s41, 4
	s_add_i32 s17, s17, -1
	s_lshl_b32 s55, s42, 4
	s_add_i32 s18, s18, -1
	s_lshl_b32 s56, s43, 4
	s_add_i32 s19, s19, -1
	s_lshl_b32 s57, s44, 4
	s_add_i32 s20, s20, -1
	s_lshl_b32 s58, s45, 4
	s_add_i32 s21, s21, -1
	s_lshl_b32 s59, s46, 4
	s_cmp_gt_i32 s23, 0
	v_cvt_f32_i32_e32 v1, s42
	s_cselect_b32 s60, s1, 0
	v_readfirstlane_b32 s1, v0
	v_add_f32_e32 v0, 0.5, v7
	v_mul_f32_e32 v0, v146, v0
	v_cvt_i32_f32_e32 v0, v0
	v_cvt_f32_i32_e32 v7, s17
	v_rcp_iflag_f32_e32 v147, v1
	s_cmp_gt_i32 s25, 0
	v_cvt_f32_i32_e32 v1, s43
	s_cselect_b32 s61, s1, 0
	v_readfirstlane_b32 s1, v0
	v_add_f32_e32 v0, 0.5, v7
	v_mul_f32_e32 v0, v147, v0
	v_cvt_i32_f32_e32 v0, v0
	v_cvt_f32_i32_e32 v7, s18
	v_rcp_iflag_f32_e32 v148, v1
	s_cmp_gt_i32 s27, 0
	v_cvt_f32_i32_e32 v1, s44
	s_cselect_b32 s62, s1, 0
	v_readfirstlane_b32 s1, v0
	v_add_f32_e32 v0, 0.5, v7
	v_mul_f32_e32 v0, v148, v0
	v_cvt_i32_f32_e32 v0, v0
	v_cvt_f32_i32_e32 v7, s19
	v_rcp_iflag_f32_e32 v149, v1
	s_cmp_gt_i32 s29, 0
	v_cvt_f32_i32_e32 v1, s45
	s_cselect_b32 s63, s1, 0
	v_readfirstlane_b32 s1, v0
	v_add_f32_e32 v0, 0.5, v7
	v_mul_f32_e32 v0, v149, v0
	v_cvt_i32_f32_e32 v0, v0
	v_cvt_f32_i32_e32 v7, s20
	v_rcp_iflag_f32_e32 v150, v1
	s_cmp_gt_i32 s31, 0
	s_cselect_b32 s64, s1, 0
	v_readfirstlane_b32 s1, v0
	v_add_f32_e32 v0, 0.5, v7
	v_mul_f32_e32 v0, v150, v0
	v_cvt_i32_f32_e32 v0, v0
	v_cvt_f32_i32_e32 v1, s46
	s_cmp_gt_i32 s33, 0
	s_cselect_b32 s65, s1, 0
	v_readfirstlane_b32 s1, v0
	v_cvt_f32_i32_e32 v0, s21
	v_rcp_iflag_f32_e32 v151, v1
	v_mov_b32_e32 v97, 0
	v_lshlrev_b32_e32 v96, 12, v101
	v_add_f32_e32 v0, 0.5, v0
	v_mul_f32_e32 v0, v151, v0
	v_cvt_i32_f32_e32 v7, v0
	v_lshlrev_b32_e32 v0, 4, v5
	v_mov_b32_e32 v1, v97
	v_lshl_add_u64 v[98:99], s[6:7], 0, v[96:97]
	s_cmp_gt_i32 s35, 0
	v_lshl_add_u64 v[104:105], s[4:5], 0, v[0:1]
	s_mov_b64 s[4:5], 0x80
	v_lshl_or_b32 v96, v2, 1, v96
	v_lshl_add_u32 v8, v103, 4, 0
	v_mul_u32_u24_e32 v3, 0x110, v101
	s_cselect_b32 s66, s1, 0
	s_cmp_gt_i32 s38, 0
	v_readfirstlane_b32 s1, v7
	v_lshl_add_u64 v[106:107], v[104:105], 0, s[4:5]
	v_lshl_add_u64 v[0:1], s[6:7], 0, v[96:97]
	s_mov_b64 s[4:5], 0x40000
	s_mov_b32 s15, 0
	v_lshlrev_b32_e32 v126, 7, v103
	v_lshlrev_b32_e32 v102, 3, v103
	v_add_u32_e32 v131, s50, v127
	v_add_u32_e32 v132, s50, v128
	v_add_u32_e32 v133, s50, v129
	v_add_u32_e32 v134, s50, v130
	s_movk_i32 s51, 0x110
	v_or_b32_e32 v135, 16, v101
	v_or_b32_e32 v136, 32, v101
	v_or_b32_e32 v137, 48, v101
	v_or_b32_e32 v138, 64, v101
	v_or_b32_e32 v139, 0x50, v101
	v_or_b32_e32 v140, 0x60, v101
	v_or_b32_e32 v141, 0x70, v101
	v_or_b32_e32 v142, 0x80, v101
	v_or_b32_e32 v143, 0x90, v101
	v_bitop3_b32 v152, v6, v101, 3 bitop3:0x78
	s_mul_i32 s67, s52, s60
	s_mul_i32 s68, s53, s61
	s_mul_i32 s69, s54, s62
	s_mul_i32 s70, s55, s63
	s_mul_i32 s71, s56, s64
	s_mul_i32 s72, s57, s65
	s_mul_i32 s73, s58, s66
	s_cselect_b32 s74, s1, 0
	v_lshl_add_u64 v[108:109], v[0:1], 0, s[4:5]
	s_lshl_b32 s6, s0, 2
	v_lshlrev_b32_e32 v153, 2, v4
	v_lshlrev_b32_e32 v96, 1, v2
	s_mov_b64 s[16:17], 0x10000
	s_mov_b64 s[18:19], 0x20000
	s_mov_b64 s[20:21], 0x30000
	s_mov_b32 s22, 0x3f3504f3
	s_mov_b32 s75, 0x3ea7ba05
	s_mov_b32 s24, 0xbfba00e3
	s_mov_b32 s26, 0x3f87dc22
	s_mov_b32 s28, 0x3fb5f0e3
	s_brev_b32 s76, -2
	v_add_u32_e32 v154, v8, v3
	s_movk_i32 s77, 0x1080
	s_mov_b32 s30, 0xbe91a98e
	s_mov_b32 s34, 0x3e827906
	s_branch .LBB2_3
.LBB2_2:
	s_or_b64 exec, exec, s[0:1]
	s_mov_b32 s48, s101
	s_add_i32 s101, s101, s49
	s_cmp_ge_i32 s48, s47
	s_cbranch_scc1 .LBB2_78
